# P2: pipelined converter, dedicated converter workgroups 72 -> 40 (216 GEMM workgroups)
# baseline (speedup 1.0000x reference)
.LBB0_178:
	s_cmp_lt_i32 s60, 3
	s_cselect_b64 s[8:9], -1, 0
	v_writelane_b32 v252, s60, 57
	s_and_b64 s[2:3], s[8:9], s[2:3]
	s_andn2_b64 vcc, exec, s[2:3]
	v_writelane_b32 v252, s61, 58
	v_writelane_b32 v252, s56, 59
	s_cbranch_vccnz .LBB0_289
	s_cmpk_gt_i32 s62, 0x7f
	s_cselect_b32 s2, 0xffffffd8, 0
	s_add_i32 s33, s2, s62
	s_mov_b32 s7, 0
	s_cmp_lt_i32 s80, s33
	s_mov_b64 s[2:3], -1
	s_cbranch_scc1 .LBB0_208
	s_load_dwordx2 s[10:11], s[0:1], 0x128
	s_load_dwordx4 s[12:15], s[0:1], 0xe8
	s_load_dwordx4 s[16:19], s[0:1], 0xf8
	s_load_dwordx4 s[20:23], s[0:1], 0x108
	v_mov_b32_e32 v1, 0x43e00000
	s_mov_b32 s27, 0xc3e00000
	v_and_b32_e32 v25, 7, v206
	v_lshrrev_b32_e32 v26, 3, v206
	v_lshlrev_b32_e32 v10, 4, v25
	v_lshlrev_b32_e32 v11, 11, v25
	v_lshlrev_b32_e32 v12, 3, v26
	v_lshlrev_b32_e32 v2, 14, v26
	v_add_u32_e32 v3, 2048, v2
	v_add_u32_e32 v4, 4096, v2
	v_add_u32_e32 v5, 6144, v2
	v_add_u32_e32 v6, 8192, v2
	v_add_u32_e32 v7, 10240, v2
	v_add_u32_e32 v8, 12288, v2
	v_add_u32_e32 v9, 14336, v2
	v_mov_b32_e32 v26, 0
	s_waitcnt lgkmcnt(0)
	s_add_u32 s46, s10, 0x14000
	s_addc_u32 s47, s11, 0
